# stack on v14: index score-loop fragment prefetch, index key-fragment loads issued up-front (counted vmcnt), RWKV-out prologue loads de-serialised, GLA-decay dot-product LDS reads grouped per block
# speedup vs baseline: 1.0017x; 1.0017x over previous
.LBB0_263:
	s_and_b32 s0, s80, 0xffffffc0
	v_add_u32_e32 v2, s0, v36
	s_movk_i32 s5, 0x3a00
	v_readlane_b32 s8, v239, 24
	s_and_b32 s1, s81, 0x180
	v_mul_lo_u32 v2, v2, s5
	v_readlane_b32 s9, v239, 25
	s_lshl_b32 s14, s1, 1
	v_mov_b32_e32 v23, v3
	v_lshl_add_u64 v[4:5], v[2:3], 1, s[8:9]
	v_lshl_add_u64 v[4:5], v[4:5], 0, s[14:15]
	v_lshl_add_u64 v[4:5], v[4:5], 0, v[22:23]
	s_mov_b32 s6, 0x12a00000
	v_add_co_u32_e32 v4, vcc, s6, v4
	v_add_u32_e32 v2, s0, v37
	s_nop 0
	v_addc_co_u32_e32 v5, vcc, 0, v5, vcc
	v_mul_lo_u32 v2, v2, s5
	global_load_dwordx4 v[8:11], v[4:5], off offset:1024
	v_lshl_add_u64 v[4:5], v[2:3], 1, s[8:9]
	v_or_b32_e32 v2, s1, v38
	v_add_u32_e32 v2, v2, v39
	v_lshl_add_u64 v[12:13], v[2:3], 2, s[22:23]
	global_load_dword v24, v[12:13], off
	v_add_u32_e32 v12, 0x800, v2
	v_mov_b32_e32 v13, v3
	v_lshl_add_u64 v[12:13], v[12:13], 2, s[22:23]
	global_load_dword v25, v[12:13], off
	v_add_u32_e32 v12, 0x1000, v2
	v_mov_b32_e32 v13, v3
	v_lshl_add_u64 v[12:13], v[12:13], 2, s[22:23]
	v_add_u32_e32 v2, 0x1800, v2
	v_lshl_add_u64 v[4:5], v[4:5], 0, s[14:15]
	global_load_dword v26, v[12:13], off
	v_lshl_add_u64 v[12:13], v[2:3], 2, s[22:23]
	v_or_b32_e32 v2, s1, v40
	v_lshl_add_u64 v[4:5], v[4:5], 0, v[22:23]
	global_load_dword v27, v[12:13], off
	v_lshl_add_u64 v[12:13], v[2:3], 2, s[24:25]
	v_or_b32_e32 v2, s0, v41
	v_add_co_u32_e32 v4, vcc, s6, v4
	v_lshlrev_b32_e32 v2, 9, v2
	s_nop 0
	v_addc_co_u32_e32 v5, vcc, 0, v5, vcc
	global_load_dword v23, v[12:13], off
	v_lshl_add_u64 v[12:13], v[2:3], 2, v[20:21]
	global_load_dwordx4 v[4:7], v[4:5], off offset:1024
	v_readlane_b32 s10, v239, 26
	global_load_dwordx4 v[12:15], v[12:13], off
	v_readlane_b32 s11, v239, 27
	s_waitcnt vmcnt(0)
	ds_write2st64_b32 v42, v24, v25 offset0:152 offset1:160
	ds_write2st64_b32 v42, v26, v27 offset0:168 offset1:176
	s_and_saveexec_b64 s[0:1], s[36:37]
	ds_write_b128 v44, v[12:15] offset:34816
	s_or_b64 exec, exec, s[0:1]
	s_waitcnt lgkmcnt(0)
	s_barrier
	ds_read2st64_b32 v[34:35], v45 offset0:152 offset1:154
	ds_read2st64_b32 v[32:33], v45 offset0:156 offset1:158
	ds_read2st64_b32 v[30:31], v45 offset0:160 offset1:162
	ds_read2st64_b32 v[28:29], v45 offset0:164 offset1:166
	ds_read2st64_b32 v[26:27], v45 offset0:168 offset1:170
	ds_read2st64_b32 v[24:25], v45 offset0:172 offset1:174
	ds_read2st64_b32 v[14:15], v45 offset0:176 offset1:178
	ds_read2st64_b32 v[12:13], v45 offset0:180 offset1:182
	ds_read_b128 v[50:53], v46 offset:34816
	ds_read_b128 v[54:57], v46 offset:34832
	ds_read_b128 v[58:61], v46 offset:34848
	ds_read_b128 v[62:65], v46 offset:34864
	s_waitcnt lgkmcnt(3)
	v_mul_f32_e32 v2, v35, v51
	v_fmac_f32_e32 v2, v34, v50
	s_waitcnt lgkmcnt(2)
	v_mul_f32_e32 v50, v31, v55
	v_fmac_f32_e32 v2, v32, v52
	v_fmac_f32_e32 v50, v30, v54
	v_fmac_f32_e32 v2, v33, v53
	v_fmac_f32_e32 v50, v28, v56
	v_add_f32_e32 v2, v23, v2
	v_fmac_f32_e32 v50, v29, v57
	v_add_f32_e32 v2, v2, v50
	s_waitcnt lgkmcnt(1)
	v_mul_f32_e32 v50, v27, v59
	v_fmac_f32_e32 v50, v26, v58
	v_fmac_f32_e32 v50, v24, v60
	v_fmac_f32_e32 v50, v25, v61
	v_add_f32_e32 v2, v2, v50
	s_waitcnt lgkmcnt(0)
	v_mul_f32_e32 v50, v15, v63
	v_fmac_f32_e32 v50, v14, v62
	v_fmac_f32_e32 v50, v12, v64
	v_fmac_f32_e32 v50, v13, v65
	v_add_f32_e32 v2, v2, v50
	v_min_f32_e32 v50, 0, v2
	v_mul_f32_e64 v2, |v2|, s35
	v_exp_f32_e32 v2, v2
	s_nop 0
	v_add_f32_e32 v2, 1.0, v2
	v_cmp_gt_f32_e32 vcc, s21, v2
	s_nop 1
	v_cndmask_b32_e64 v51, 0, 32, vcc
	v_ldexp_f32 v2, v2, v51
	v_log_f32_e32 v2, v2
	s_nop 0
	v_mul_f32_e32 v51, 0x3f317217, v2
	v_fma_f32 v51, v2, s33, -v51
	v_fmac_f32_e32 v51, 0x3377d1cf, v2
	v_fmac_f32_e32 v51, 0x3f317217, v2
	v_cmp_lt_f32_e64 s[0:1], |v2|, s63
	s_nop 1
	v_cndmask_b32_e64 v2, v2, v51, s[0:1]
	v_cndmask_b32_e32 v51, 0, v215, vcc
	v_sub_f32_e32 v2, v2, v51
	v_sub_f32_e32 v2, v50, v2
	ds_read_b128 v[240:243], v46 offset:34880
	ds_read_b128 v[244:247], v46 offset:34896
	ds_read_b128 v[248:251], v46 offset:34912
	ds_read_b128 v[252:255], v46 offset:34928
	s_mov_b32 s0, 0x3d800000
	v_fma_f32 v2, v2, s0, 0
	s_waitcnt lgkmcnt(3)
	v_mul_f32_e32 v51, v35, v241
	v_fmac_f32_e32 v51, v34, v240
	v_fmac_f32_e32 v51, v32, v242
	v_fmac_f32_e32 v51, v33, v243
	v_add_f32_e32 v54, v23, v51
	s_waitcnt lgkmcnt(2)
	v_mul_f32_e32 v51, v31, v245
	v_fmac_f32_e32 v51, v30, v244
	v_fmac_f32_e32 v51, v28, v246
	v_fmac_f32_e32 v51, v29, v247
	v_add_f32_e32 v54, v54, v51
	s_waitcnt lgkmcnt(1)
	v_mul_f32_e32 v51, v27, v249
	v_fmac_f32_e32 v51, v26, v248
	v_fmac_f32_e32 v51, v24, v250
	v_fmac_f32_e32 v51, v25, v251
	v_add_f32_e32 v54, v54, v51
	s_waitcnt lgkmcnt(0)
	v_mul_f32_e32 v51, v15, v253
	v_fmac_f32_e32 v51, v14, v252
	v_fmac_f32_e32 v51, v12, v254
	v_fmac_f32_e32 v51, v13, v255
	v_add_f32_e32 v50, v54, v51
	v_min_f32_e32 v51, 0, v50
	v_mul_f32_e64 v50, |v50|, s35
	v_exp_f32_e32 v50, v50
	s_nop 0
	v_add_f32_e32 v50, 1.0, v50
	v_cmp_gt_f32_e32 vcc, s21, v50
	s_nop 1
	v_cndmask_b32_e64 v52, 0, 32, vcc
	v_ldexp_f32 v50, v50, v52
	v_log_f32_e32 v50, v50
	s_nop 0
	v_mul_f32_e32 v52, 0x3f317217, v50
	v_fma_f32 v52, v50, s33, -v52
	v_fmac_f32_e32 v52, 0x3377d1cf, v50
	v_fmac_f32_e32 v52, 0x3f317217, v50
	v_cmp_lt_f32_e64 s[0:1], |v50|, s63
	s_nop 1
	v_cndmask_b32_e64 v50, v50, v52, s[0:1]
	v_cndmask_b32_e32 v52, 0, v215, vcc
	v_sub_f32_e32 v50, v50, v52
	ds_read_b128 v[240:243], v46 offset:34944
	ds_read_b128 v[244:247], v46 offset:34960
	ds_read_b128 v[248:251], v46 offset:34976
	ds_read_b128 v[252:255], v46 offset:34992
	v_sub_f32_e32 v50, v51, v50
	v_fmamk_f32 v50, v50, 0x3d800000, v2
	s_waitcnt lgkmcnt(3)
	v_mul_f32_e32 v51, v35, v241
	v_fmac_f32_e32 v51, v34, v240
	v_fmac_f32_e32 v51, v32, v242
	v_fmac_f32_e32 v51, v33, v243
	v_add_f32_e32 v51, v23, v51
	s_waitcnt lgkmcnt(2)
	v_mul_f32_e32 v53, v31, v245
	v_fmac_f32_e32 v53, v30, v244
	v_fmac_f32_e32 v53, v28, v246
	v_fmac_f32_e32 v53, v29, v247
	v_add_f32_e32 v51, v51, v53
	s_waitcnt lgkmcnt(1)
	v_mul_f32_e32 v53, v27, v249
	v_fmac_f32_e32 v53, v26, v248
	v_fmac_f32_e32 v53, v24, v250
	v_fmac_f32_e32 v53, v25, v251
	v_add_f32_e32 v51, v51, v53
	s_waitcnt lgkmcnt(0)
	v_mul_f32_e32 v53, v15, v253
	v_fmac_f32_e32 v53, v14, v252
	v_fmac_f32_e32 v53, v12, v254
	v_fmac_f32_e32 v53, v13, v255
	v_add_f32_e32 v51, v51, v53
	v_min_f32_e32 v52, 0, v51
	v_mul_f32_e64 v51, |v51|, s35
	v_exp_f32_e32 v51, v51
	s_nop 0
	v_add_f32_e32 v51, 1.0, v51
	v_cmp_gt_f32_e32 vcc, s21, v51
	s_nop 1
	v_cndmask_b32_e64 v53, 0, 32, vcc
	v_ldexp_f32 v51, v51, v53
	v_log_f32_e32 v51, v51
	s_nop 0
	v_mul_f32_e32 v53, 0x3f317217, v51
	v_fma_f32 v53, v51, s33, -v53
	v_fmac_f32_e32 v53, 0x3377d1cf, v51
	v_fmac_f32_e32 v53, 0x3f317217, v51
	v_cmp_lt_f32_e64 s[0:1], |v51|, s63
	s_nop 1
	v_cndmask_b32_e64 v51, v51, v53, s[0:1]
	v_cndmask_b32_e32 v53, 0, v215, vcc
	v_sub_f32_e32 v51, v51, v53
	v_sub_f32_e32 v51, v52, v51
	ds_read_b128 v[240:243], v46 offset:35008
	ds_read_b128 v[244:247], v46 offset:35024
	ds_read_b128 v[248:251], v46 offset:35040
	ds_read_b128 v[252:255], v46 offset:35056
	v_fmamk_f32 v51, v51, 0x3d800000, v50
	s_waitcnt lgkmcnt(3)
	v_mul_f32_e32 v53, v35, v241
	v_fmac_f32_e32 v53, v34, v240
	v_fmac_f32_e32 v53, v32, v242
	v_fmac_f32_e32 v53, v33, v243
	v_add_f32_e32 v56, v23, v53
	s_waitcnt lgkmcnt(2)
	v_mul_f32_e32 v53, v31, v245
	v_fmac_f32_e32 v53, v30, v244
	v_fmac_f32_e32 v53, v28, v246
	v_fmac_f32_e32 v53, v29, v247
	v_add_f32_e32 v56, v56, v53
	s_waitcnt lgkmcnt(1)
	v_mul_f32_e32 v53, v27, v249
	v_fmac_f32_e32 v53, v26, v248
	v_fmac_f32_e32 v53, v24, v250
	v_fmac_f32_e32 v53, v25, v251
	v_add_f32_e32 v56, v56, v53
	s_waitcnt lgkmcnt(0)
	v_mul_f32_e32 v53, v15, v253
	v_fmac_f32_e32 v53, v14, v252
	v_fmac_f32_e32 v53, v12, v254
	v_fmac_f32_e32 v53, v13, v255
	v_add_f32_e32 v52, v56, v53
	v_min_f32_e32 v53, 0, v52
	v_mul_f32_e64 v52, |v52|, s35
	v_exp_f32_e32 v52, v52
	s_nop 0
	v_add_f32_e32 v52, 1.0, v52
	v_cmp_gt_f32_e32 vcc, s21, v52
	s_nop 1
	v_cndmask_b32_e64 v54, 0, 32, vcc
	v_ldexp_f32 v52, v52, v54
	v_log_f32_e32 v52, v52
	s_nop 0
	v_mul_f32_e32 v54, 0x3f317217, v52
	v_fma_f32 v54, v52, s33, -v54
	v_fmac_f32_e32 v54, 0x3377d1cf, v52
	v_fmac_f32_e32 v54, 0x3f317217, v52
	v_cmp_lt_f32_e64 s[0:1], |v52|, s63
	s_nop 1
	v_cndmask_b32_e64 v52, v52, v54, s[0:1]
	v_cndmask_b32_e32 v54, 0, v215, vcc
	v_sub_f32_e32 v52, v52, v54
	ds_read_b128 v[240:243], v46 offset:35072
	ds_read_b128 v[244:247], v46 offset:35088
	ds_read_b128 v[248:251], v46 offset:35104
	ds_read_b128 v[252:255], v46 offset:35120
	v_sub_f32_e32 v52, v53, v52
	v_fmamk_f32 v52, v52, 0x3d800000, v51
	s_waitcnt lgkmcnt(3)
	v_mul_f32_e32 v53, v35, v241
	v_fmac_f32_e32 v53, v34, v240
	v_fmac_f32_e32 v53, v32, v242
	v_fmac_f32_e32 v53, v33, v243
	v_add_f32_e32 v53, v23, v53
	s_waitcnt lgkmcnt(2)
	v_mul_f32_e32 v55, v31, v245
	v_fmac_f32_e32 v55, v30, v244
	v_fmac_f32_e32 v55, v28, v246
	v_fmac_f32_e32 v55, v29, v247
	v_add_f32_e32 v53, v53, v55
	s_waitcnt lgkmcnt(1)
	v_mul_f32_e32 v55, v27, v249
	v_fmac_f32_e32 v55, v26, v248
	v_fmac_f32_e32 v55, v24, v250
	v_fmac_f32_e32 v55, v25, v251
	v_add_f32_e32 v53, v53, v55
	s_waitcnt lgkmcnt(0)
	v_mul_f32_e32 v55, v15, v253
	v_fmac_f32_e32 v55, v14, v252
	v_fmac_f32_e32 v55, v12, v254
	v_fmac_f32_e32 v55, v13, v255
	v_add_f32_e32 v53, v53, v55
	v_min_f32_e32 v54, 0, v53
	v_mul_f32_e64 v53, |v53|, s35
	v_exp_f32_e32 v53, v53
	s_nop 0
	v_add_f32_e32 v53, 1.0, v53
	v_cmp_gt_f32_e32 vcc, s21, v53
	s_nop 1
	v_cndmask_b32_e64 v55, 0, 32, vcc
	v_ldexp_f32 v53, v53, v55
	v_log_f32_e32 v53, v53
	s_nop 0
	v_mul_f32_e32 v55, 0x3f317217, v53
	v_fma_f32 v55, v53, s33, -v55
	v_fmac_f32_e32 v55, 0x3377d1cf, v53
	v_fmac_f32_e32 v55, 0x3f317217, v53
	v_cmp_lt_f32_e64 s[0:1], |v53|, s63
	s_nop 1
	v_cndmask_b32_e64 v53, v53, v55, s[0:1]
	v_cndmask_b32_e32 v55, 0, v215, vcc
	v_sub_f32_e32 v53, v53, v55
	v_sub_f32_e32 v53, v54, v53
	ds_read_b128 v[240:243], v46 offset:35136
	ds_read_b128 v[244:247], v46 offset:35152
	ds_read_b128 v[248:251], v46 offset:35168
	ds_read_b128 v[252:255], v46 offset:35184
	v_fmamk_f32 v53, v53, 0x3d800000, v52
	s_waitcnt lgkmcnt(3)
	v_mul_f32_e32 v55, v35, v241
	v_fmac_f32_e32 v55, v34, v240
	v_fmac_f32_e32 v55, v32, v242
	v_fmac_f32_e32 v55, v33, v243
	v_add_f32_e32 v58, v23, v55
	s_waitcnt lgkmcnt(2)
	v_mul_f32_e32 v55, v31, v245
	v_fmac_f32_e32 v55, v30, v244
	v_fmac_f32_e32 v55, v28, v246
	v_fmac_f32_e32 v55, v29, v247
	v_add_f32_e32 v58, v58, v55
	s_waitcnt lgkmcnt(1)
	v_mul_f32_e32 v55, v27, v249
	v_fmac_f32_e32 v55, v26, v248
	v_fmac_f32_e32 v55, v24, v250
	v_fmac_f32_e32 v55, v25, v251
	v_add_f32_e32 v58, v58, v55
	s_waitcnt lgkmcnt(0)
	v_mul_f32_e32 v55, v15, v253
	v_fmac_f32_e32 v55, v14, v252
	v_fmac_f32_e32 v55, v12, v254
	v_fmac_f32_e32 v55, v13, v255
	v_add_f32_e32 v54, v58, v55
	v_min_f32_e32 v55, 0, v54
	v_mul_f32_e64 v54, |v54|, s35
	v_exp_f32_e32 v54, v54
	s_nop 0
	v_add_f32_e32 v54, 1.0, v54
	v_cmp_gt_f32_e32 vcc, s21, v54
	s_nop 1
	v_cndmask_b32_e64 v56, 0, 32, vcc
	v_ldexp_f32 v54, v54, v56
	v_log_f32_e32 v54, v54
	s_nop 0
	v_mul_f32_e32 v56, 0x3f317217, v54
	v_fma_f32 v56, v54, s33, -v56
	v_fmac_f32_e32 v56, 0x3377d1cf, v54
	v_fmac_f32_e32 v56, 0x3f317217, v54
	v_cmp_lt_f32_e64 s[0:1], |v54|, s63
	s_nop 1
	v_cndmask_b32_e64 v54, v54, v56, s[0:1]
	v_cndmask_b32_e32 v56, 0, v215, vcc
	v_sub_f32_e32 v54, v54, v56
	ds_read_b128 v[240:243], v46 offset:35200
	ds_read_b128 v[244:247], v46 offset:35216
	ds_read_b128 v[248:251], v46 offset:35232
	ds_read_b128 v[252:255], v46 offset:35248
	v_sub_f32_e32 v54, v55, v54
	v_fmamk_f32 v54, v54, 0x3d800000, v53
	s_waitcnt lgkmcnt(3)
	v_mul_f32_e32 v55, v35, v241
	v_fmac_f32_e32 v55, v34, v240
	v_fmac_f32_e32 v55, v32, v242
	v_fmac_f32_e32 v55, v33, v243
	v_add_f32_e32 v55, v23, v55
	s_waitcnt lgkmcnt(2)
	v_mul_f32_e32 v57, v31, v245
	v_fmac_f32_e32 v57, v30, v244
	v_fmac_f32_e32 v57, v28, v246
	v_fmac_f32_e32 v57, v29, v247
	v_add_f32_e32 v55, v55, v57
	s_waitcnt lgkmcnt(1)
	v_mul_f32_e32 v57, v27, v249
	v_fmac_f32_e32 v57, v26, v248
	v_fmac_f32_e32 v57, v24, v250
	v_fmac_f32_e32 v57, v25, v251
	v_add_f32_e32 v55, v55, v57
	s_waitcnt lgkmcnt(0)
	v_mul_f32_e32 v57, v15, v253
	v_fmac_f32_e32 v57, v14, v252
	v_fmac_f32_e32 v57, v12, v254
	v_fmac_f32_e32 v57, v13, v255
	v_add_f32_e32 v55, v55, v57
	v_min_f32_e32 v56, 0, v55
	v_mul_f32_e64 v55, |v55|, s35
	v_exp_f32_e32 v55, v55
	s_nop 0
	v_add_f32_e32 v55, 1.0, v55
	v_cmp_gt_f32_e32 vcc, s21, v55
	s_nop 1
	v_cndmask_b32_e64 v57, 0, 32, vcc
	v_ldexp_f32 v55, v55, v57
	v_log_f32_e32 v55, v55
	s_nop 0
	v_mul_f32_e32 v57, 0x3f317217, v55
	v_fma_f32 v57, v55, s33, -v57
	v_fmac_f32_e32 v57, 0x3377d1cf, v55
	v_fmac_f32_e32 v57, 0x3f317217, v55
	v_cmp_lt_f32_e64 s[0:1], |v55|, s63
	s_nop 1
	v_cndmask_b32_e64 v55, v55, v57, s[0:1]
	v_cndmask_b32_e32 v57, 0, v215, vcc
	v_sub_f32_e32 v55, v55, v57
	v_sub_f32_e32 v55, v56, v55
	ds_read_b128 v[240:243], v46 offset:35264
	ds_read_b128 v[244:247], v46 offset:35280
	ds_read_b128 v[248:251], v46 offset:35296
	ds_read_b128 v[252:255], v46 offset:35312
	v_fmamk_f32 v55, v55, 0x3d800000, v54
	s_waitcnt lgkmcnt(3)
	v_mul_f32_e32 v57, v35, v241
	v_fmac_f32_e32 v57, v34, v240
	v_fmac_f32_e32 v57, v32, v242
	v_fmac_f32_e32 v57, v33, v243
	v_add_f32_e32 v60, v23, v57
	s_waitcnt lgkmcnt(2)
	v_mul_f32_e32 v57, v31, v245
	v_fmac_f32_e32 v57, v30, v244
	v_fmac_f32_e32 v57, v28, v246
	v_fmac_f32_e32 v57, v29, v247
	v_add_f32_e32 v60, v60, v57
	s_waitcnt lgkmcnt(1)
	v_mul_f32_e32 v57, v27, v249
	v_fmac_f32_e32 v57, v26, v248
	v_fmac_f32_e32 v57, v24, v250
	v_fmac_f32_e32 v57, v25, v251
	v_add_f32_e32 v60, v60, v57
	s_waitcnt lgkmcnt(0)
	v_mul_f32_e32 v57, v15, v253
	v_fmac_f32_e32 v57, v14, v252
	v_fmac_f32_e32 v57, v12, v254
	v_fmac_f32_e32 v57, v13, v255
	v_add_f32_e32 v56, v60, v57
	v_min_f32_e32 v57, 0, v56
	v_mul_f32_e64 v56, |v56|, s35
	v_exp_f32_e32 v56, v56
	s_nop 0
	v_add_f32_e32 v56, 1.0, v56
	v_cmp_gt_f32_e32 vcc, s21, v56
	s_nop 1
	v_cndmask_b32_e64 v58, 0, 32, vcc
	v_ldexp_f32 v56, v56, v58
	v_log_f32_e32 v56, v56
	s_nop 0
	v_mul_f32_e32 v58, 0x3f317217, v56
	v_fma_f32 v58, v56, s33, -v58
	v_fmac_f32_e32 v58, 0x3377d1cf, v56
	v_fmac_f32_e32 v58, 0x3f317217, v56
	v_cmp_lt_f32_e64 s[0:1], |v56|, s63
	s_nop 1
	v_cndmask_b32_e64 v56, v56, v58, s[0:1]
	v_cndmask_b32_e32 v58, 0, v215, vcc
	v_sub_f32_e32 v56, v56, v58
	ds_read_b128 v[240:243], v46 offset:35328
	ds_read_b128 v[244:247], v46 offset:35344
	ds_read_b128 v[248:251], v46 offset:35360
	ds_read_b128 v[252:255], v46 offset:35376
	v_sub_f32_e32 v56, v57, v56
	v_fmamk_f32 v56, v56, 0x3d800000, v55
	s_waitcnt lgkmcnt(3)
	v_mul_f32_e32 v57, v35, v241
	v_fmac_f32_e32 v57, v34, v240
	v_fmac_f32_e32 v57, v32, v242
	v_fmac_f32_e32 v57, v33, v243
	v_add_f32_e32 v57, v23, v57
	s_waitcnt lgkmcnt(2)
	v_mul_f32_e32 v59, v31, v245
	v_fmac_f32_e32 v59, v30, v244
	v_fmac_f32_e32 v59, v28, v246
	v_fmac_f32_e32 v59, v29, v247
	v_add_f32_e32 v57, v57, v59
	s_waitcnt lgkmcnt(1)
	v_mul_f32_e32 v59, v27, v249
	v_fmac_f32_e32 v59, v26, v248
	v_fmac_f32_e32 v59, v24, v250
	v_fmac_f32_e32 v59, v25, v251
	v_add_f32_e32 v57, v57, v59
	s_waitcnt lgkmcnt(0)
	v_mul_f32_e32 v59, v15, v253
	v_fmac_f32_e32 v59, v14, v252
	v_fmac_f32_e32 v59, v12, v254
	v_fmac_f32_e32 v59, v13, v255
	v_add_f32_e32 v57, v57, v59
	v_min_f32_e32 v58, 0, v57
	v_mul_f32_e64 v57, |v57|, s35
	v_exp_f32_e32 v57, v57
	s_nop 0
	v_add_f32_e32 v57, 1.0, v57
	v_cmp_gt_f32_e32 vcc, s21, v57
	s_nop 1
	v_cndmask_b32_e64 v59, 0, 32, vcc
	v_ldexp_f32 v57, v57, v59
	v_log_f32_e32 v57, v57
	s_nop 0
	v_mul_f32_e32 v59, 0x3f317217, v57
	v_fma_f32 v59, v57, s33, -v59
	v_fmac_f32_e32 v59, 0x3377d1cf, v57
	v_fmac_f32_e32 v59, 0x3f317217, v57
	v_cmp_lt_f32_e64 s[0:1], |v57|, s63
	s_nop 1
	v_cndmask_b32_e64 v57, v57, v59, s[0:1]
	v_cndmask_b32_e32 v59, 0, v215, vcc
	v_sub_f32_e32 v57, v57, v59
	v_sub_f32_e32 v57, v58, v57
	ds_read_b128 v[240:243], v46 offset:35392
	ds_read_b128 v[244:247], v46 offset:35408
	ds_read_b128 v[248:251], v46 offset:35424
	ds_read_b128 v[252:255], v46 offset:35440
	v_fmamk_f32 v57, v57, 0x3d800000, v56
	s_waitcnt lgkmcnt(3)
	v_mul_f32_e32 v59, v35, v241
	v_fmac_f32_e32 v59, v34, v240
	v_fmac_f32_e32 v59, v32, v242
	v_fmac_f32_e32 v59, v33, v243
	v_add_f32_e32 v62, v23, v59
	s_waitcnt lgkmcnt(2)
	v_mul_f32_e32 v59, v31, v245
	v_fmac_f32_e32 v59, v30, v244
	v_fmac_f32_e32 v59, v28, v246
	v_fmac_f32_e32 v59, v29, v247
	v_add_f32_e32 v62, v62, v59
	s_waitcnt lgkmcnt(1)
	v_mul_f32_e32 v59, v27, v249
	v_fmac_f32_e32 v59, v26, v248
	v_fmac_f32_e32 v59, v24, v250
	v_fmac_f32_e32 v59, v25, v251
	v_add_f32_e32 v62, v62, v59
	s_waitcnt lgkmcnt(0)
	v_mul_f32_e32 v59, v15, v253
	v_fmac_f32_e32 v59, v14, v252
	v_fmac_f32_e32 v59, v12, v254
	v_fmac_f32_e32 v59, v13, v255
	v_add_f32_e32 v58, v62, v59
	v_min_f32_e32 v59, 0, v58
	v_mul_f32_e64 v58, |v58|, s35
	v_exp_f32_e32 v58, v58
	s_nop 0
	v_add_f32_e32 v58, 1.0, v58
	v_cmp_gt_f32_e32 vcc, s21, v58
	s_nop 1
	v_cndmask_b32_e64 v60, 0, 32, vcc
	v_ldexp_f32 v58, v58, v60
	v_log_f32_e32 v58, v58
	s_nop 0
	v_mul_f32_e32 v60, 0x3f317217, v58
	v_fma_f32 v60, v58, s33, -v60
	v_fmac_f32_e32 v60, 0x3377d1cf, v58
	v_fmac_f32_e32 v60, 0x3f317217, v58
	v_cmp_lt_f32_e64 s[0:1], |v58|, s63
	s_nop 1
	v_cndmask_b32_e64 v58, v58, v60, s[0:1]
	v_cndmask_b32_e32 v60, 0, v215, vcc
	v_sub_f32_e32 v58, v58, v60
	ds_read_b128 v[240:243], v46 offset:35456
	ds_read_b128 v[244:247], v46 offset:35472
	ds_read_b128 v[248:251], v46 offset:35488
	ds_read_b128 v[252:255], v46 offset:35504
	v_sub_f32_e32 v58, v59, v58
	v_fmamk_f32 v58, v58, 0x3d800000, v57
	s_waitcnt lgkmcnt(3)
	v_mul_f32_e32 v59, v35, v241
	v_fmac_f32_e32 v59, v34, v240
	v_fmac_f32_e32 v59, v32, v242
	v_fmac_f32_e32 v59, v33, v243
	v_add_f32_e32 v59, v23, v59
	s_waitcnt lgkmcnt(2)
	v_mul_f32_e32 v61, v31, v245
	v_fmac_f32_e32 v61, v30, v244
	v_fmac_f32_e32 v61, v28, v246
	v_fmac_f32_e32 v61, v29, v247
	v_add_f32_e32 v59, v59, v61
	s_waitcnt lgkmcnt(1)
	v_mul_f32_e32 v61, v27, v249
	v_fmac_f32_e32 v61, v26, v248
	v_fmac_f32_e32 v61, v24, v250
	v_fmac_f32_e32 v61, v25, v251
	v_add_f32_e32 v59, v59, v61
	s_waitcnt lgkmcnt(0)
	v_mul_f32_e32 v61, v15, v253
	v_fmac_f32_e32 v61, v14, v252
	v_fmac_f32_e32 v61, v12, v254
	v_fmac_f32_e32 v61, v13, v255
	v_add_f32_e32 v59, v59, v61
	v_min_f32_e32 v60, 0, v59
	v_mul_f32_e64 v59, |v59|, s35
	v_exp_f32_e32 v59, v59
	s_nop 0
	v_add_f32_e32 v59, 1.0, v59
	v_cmp_gt_f32_e32 vcc, s21, v59
	s_nop 1
	v_cndmask_b32_e64 v61, 0, 32, vcc
	v_ldexp_f32 v59, v59, v61
	v_log_f32_e32 v59, v59
	s_nop 0
	v_mul_f32_e32 v61, 0x3f317217, v59
	v_fma_f32 v61, v59, s33, -v61
	v_fmac_f32_e32 v61, 0x3377d1cf, v59
	v_fmac_f32_e32 v61, 0x3f317217, v59
	v_cmp_lt_f32_e64 s[0:1], |v59|, s63
	s_nop 1
	v_cndmask_b32_e64 v59, v59, v61, s[0:1]
	v_cndmask_b32_e32 v61, 0, v215, vcc
	v_sub_f32_e32 v59, v59, v61
	v_sub_f32_e32 v59, v60, v59
	ds_read_b128 v[240:243], v46 offset:35520
	ds_read_b128 v[244:247], v46 offset:35536
	ds_read_b128 v[248:251], v46 offset:35552
	ds_read_b128 v[252:255], v46 offset:35568
	v_fmamk_f32 v59, v59, 0x3d800000, v58
	s_waitcnt lgkmcnt(3)
	v_mul_f32_e32 v61, v35, v241
	v_fmac_f32_e32 v61, v34, v240
	v_fmac_f32_e32 v61, v32, v242
	v_fmac_f32_e32 v61, v33, v243
	v_add_f32_e32 v64, v23, v61
	s_waitcnt lgkmcnt(2)
	v_mul_f32_e32 v61, v31, v245
	v_fmac_f32_e32 v61, v30, v244
	v_fmac_f32_e32 v61, v28, v246
	v_fmac_f32_e32 v61, v29, v247
	v_add_f32_e32 v64, v64, v61
	s_waitcnt lgkmcnt(1)
	v_mul_f32_e32 v61, v27, v249
	v_fmac_f32_e32 v61, v26, v248
	v_fmac_f32_e32 v61, v24, v250
	v_fmac_f32_e32 v61, v25, v251
	v_add_f32_e32 v64, v64, v61
	s_waitcnt lgkmcnt(0)
	v_mul_f32_e32 v61, v15, v253
	v_fmac_f32_e32 v61, v14, v252
	v_fmac_f32_e32 v61, v12, v254
	v_fmac_f32_e32 v61, v13, v255
	v_add_f32_e32 v60, v64, v61
	v_min_f32_e32 v61, 0, v60
	v_mul_f32_e64 v60, |v60|, s35
	v_exp_f32_e32 v60, v60
	s_nop 0
	v_add_f32_e32 v60, 1.0, v60
	v_cmp_gt_f32_e32 vcc, s21, v60
	s_nop 1
	v_cndmask_b32_e64 v62, 0, 32, vcc
	v_ldexp_f32 v60, v60, v62
	v_log_f32_e32 v60, v60
	s_nop 0
	v_mul_f32_e32 v62, 0x3f317217, v60
	v_fma_f32 v62, v60, s33, -v62
	v_fmac_f32_e32 v62, 0x3377d1cf, v60
	v_fmac_f32_e32 v62, 0x3f317217, v60
	v_cmp_lt_f32_e64 s[0:1], |v60|, s63
	s_nop 1
	v_cndmask_b32_e64 v60, v60, v62, s[0:1]
	v_cndmask_b32_e32 v62, 0, v215, vcc
	v_sub_f32_e32 v60, v60, v62
	ds_read_b128 v[240:243], v46 offset:35584
	ds_read_b128 v[244:247], v46 offset:35600
	ds_read_b128 v[248:251], v46 offset:35616
	ds_read_b128 v[252:255], v46 offset:35632
	v_sub_f32_e32 v60, v61, v60
	v_fmamk_f32 v60, v60, 0x3d800000, v59
	s_waitcnt lgkmcnt(3)
	v_mul_f32_e32 v61, v35, v241
	v_fmac_f32_e32 v61, v34, v240
	v_fmac_f32_e32 v61, v32, v242
	v_fmac_f32_e32 v61, v33, v243
	v_add_f32_e32 v61, v23, v61
	s_waitcnt lgkmcnt(2)
	v_mul_f32_e32 v63, v31, v245
	v_fmac_f32_e32 v63, v30, v244
	v_fmac_f32_e32 v63, v28, v246
	v_fmac_f32_e32 v63, v29, v247
	v_add_f32_e32 v61, v61, v63
	s_waitcnt lgkmcnt(1)
	v_mul_f32_e32 v63, v27, v249
	v_fmac_f32_e32 v63, v26, v248
	v_fmac_f32_e32 v63, v24, v250
	v_fmac_f32_e32 v63, v25, v251
	v_add_f32_e32 v61, v61, v63
	s_waitcnt lgkmcnt(0)
	v_mul_f32_e32 v63, v15, v253
	v_fmac_f32_e32 v63, v14, v252
	v_fmac_f32_e32 v63, v12, v254
	v_fmac_f32_e32 v63, v13, v255
	v_add_f32_e32 v61, v61, v63
	v_min_f32_e32 v62, 0, v61
	v_mul_f32_e64 v61, |v61|, s35
	v_exp_f32_e32 v61, v61
	s_nop 0
	v_add_f32_e32 v61, 1.0, v61
	v_cmp_gt_f32_e32 vcc, s21, v61
	s_nop 1
	v_cndmask_b32_e64 v63, 0, 32, vcc
	v_ldexp_f32 v61, v61, v63
	v_log_f32_e32 v61, v61
	s_nop 0
	v_mul_f32_e32 v63, 0x3f317217, v61
	v_fma_f32 v63, v61, s33, -v63
	v_fmac_f32_e32 v63, 0x3377d1cf, v61
	v_fmac_f32_e32 v63, 0x3f317217, v61
	v_cmp_lt_f32_e64 s[0:1], |v61|, s63
	s_nop 1
	v_cndmask_b32_e64 v61, v61, v63, s[0:1]
	v_cndmask_b32_e32 v63, 0, v215, vcc
	v_sub_f32_e32 v61, v61, v63
	v_sub_f32_e32 v61, v62, v61
	ds_read_b128 v[240:243], v46 offset:35648
	ds_read_b128 v[244:247], v46 offset:35664
	ds_read_b128 v[248:251], v46 offset:35680
	ds_read_b128 v[252:255], v46 offset:35696
	v_fmamk_f32 v61, v61, 0x3d800000, v60
	s_waitcnt lgkmcnt(3)
	v_mul_f32_e32 v63, v35, v241
	v_fmac_f32_e32 v63, v34, v240
	v_fmac_f32_e32 v63, v32, v242
	v_fmac_f32_e32 v63, v33, v243
	v_add_f32_e32 v66, v23, v63
	s_waitcnt lgkmcnt(2)
	v_mul_f32_e32 v63, v31, v245
	v_fmac_f32_e32 v63, v30, v244
	v_fmac_f32_e32 v63, v28, v246
	v_fmac_f32_e32 v63, v29, v247
	v_add_f32_e32 v66, v66, v63
	s_waitcnt lgkmcnt(1)
	v_mul_f32_e32 v63, v27, v249
	v_fmac_f32_e32 v63, v26, v248
	v_fmac_f32_e32 v63, v24, v250
	v_fmac_f32_e32 v63, v25, v251
	v_add_f32_e32 v66, v66, v63
	s_waitcnt lgkmcnt(0)
	v_mul_f32_e32 v63, v15, v253
	v_fmac_f32_e32 v63, v14, v252
	v_fmac_f32_e32 v63, v12, v254
	v_fmac_f32_e32 v63, v13, v255
	v_add_f32_e32 v62, v66, v63
	v_min_f32_e32 v63, 0, v62
	v_mul_f32_e64 v62, |v62|, s35
	v_exp_f32_e32 v62, v62
	s_nop 0
	v_add_f32_e32 v62, 1.0, v62
	v_cmp_gt_f32_e32 vcc, s21, v62
	s_nop 1
	v_cndmask_b32_e64 v64, 0, 32, vcc
	v_ldexp_f32 v62, v62, v64
	v_log_f32_e32 v62, v62
	s_nop 0
	v_mul_f32_e32 v64, 0x3f317217, v62
	v_fma_f32 v64, v62, s33, -v64
	v_fmac_f32_e32 v64, 0x3377d1cf, v62
	v_fmac_f32_e32 v64, 0x3f317217, v62
	v_cmp_lt_f32_e64 s[0:1], |v62|, s63
	s_nop 1
	v_cndmask_b32_e64 v62, v62, v64, s[0:1]
	v_cndmask_b32_e32 v64, 0, v215, vcc
	v_sub_f32_e32 v62, v62, v64
	ds_read_b128 v[240:243], v46 offset:35712
	ds_read_b128 v[244:247], v46 offset:35728
	ds_read_b128 v[248:251], v46 offset:35744
	ds_read_b128 v[252:255], v46 offset:35760
	v_sub_f32_e32 v62, v63, v62
	v_fmamk_f32 v62, v62, 0x3d800000, v61
	s_waitcnt lgkmcnt(3)
	v_mul_f32_e32 v63, v35, v241
	v_fmac_f32_e32 v63, v34, v240
	v_fmac_f32_e32 v63, v32, v242
	v_fmac_f32_e32 v63, v33, v243
	v_add_f32_e32 v63, v23, v63
	s_waitcnt lgkmcnt(2)
	v_mul_f32_e32 v65, v31, v245
	v_fmac_f32_e32 v65, v30, v244
	v_fmac_f32_e32 v65, v28, v246
	v_fmac_f32_e32 v65, v29, v247
	v_add_f32_e32 v63, v63, v65
	s_waitcnt lgkmcnt(1)
	v_mul_f32_e32 v65, v27, v249
	v_fmac_f32_e32 v65, v26, v248
	v_fmac_f32_e32 v65, v24, v250
	v_fmac_f32_e32 v65, v25, v251
	v_add_f32_e32 v63, v63, v65
	s_waitcnt lgkmcnt(0)
	v_mul_f32_e32 v65, v15, v253
	v_fmac_f32_e32 v65, v14, v252
	v_fmac_f32_e32 v65, v12, v254
	v_fmac_f32_e32 v65, v13, v255
	v_add_f32_e32 v63, v63, v65
	v_min_f32_e32 v64, 0, v63
	v_mul_f32_e64 v63, |v63|, s35
	v_exp_f32_e32 v63, v63
	s_nop 0
	v_add_f32_e32 v63, 1.0, v63
	v_cmp_gt_f32_e32 vcc, s21, v63
	s_nop 1
	v_cndmask_b32_e64 v65, 0, 32, vcc
	v_ldexp_f32 v63, v63, v65
	v_log_f32_e32 v63, v63
	s_nop 0
	v_mul_f32_e32 v65, 0x3f317217, v63
	v_fma_f32 v65, v63, s33, -v65
	v_fmac_f32_e32 v65, 0x3377d1cf, v63
	v_fmac_f32_e32 v65, 0x3f317217, v63
	v_cmp_lt_f32_e64 s[0:1], |v63|, s63
	s_nop 1
	v_cndmask_b32_e64 v63, v63, v65, s[0:1]
	v_cndmask_b32_e32 v65, 0, v215, vcc
	v_sub_f32_e32 v63, v63, v65
	v_sub_f32_e32 v63, v64, v63
	ds_read_b128 v[240:243], v46 offset:35776
	ds_read_b128 v[244:247], v46 offset:35792
	ds_read_b128 v[248:251], v46 offset:35808
	ds_read_b128 v[252:255], v46 offset:35824
	v_fmamk_f32 v63, v63, 0x3d800000, v62
	s_waitcnt lgkmcnt(3)
	v_mul_f32_e32 v35, v35, v241
	v_fmac_f32_e32 v35, v34, v240
	v_fmac_f32_e32 v35, v32, v242
	v_fmac_f32_e32 v35, v33, v243
	v_add_f32_e32 v23, v23, v35
	s_waitcnt lgkmcnt(2)
	v_mul_f32_e32 v31, v31, v245
	v_fmac_f32_e32 v31, v30, v244
	v_fmac_f32_e32 v31, v28, v246
	v_fmac_f32_e32 v31, v29, v247
	v_add_f32_e32 v23, v23, v31
	s_waitcnt lgkmcnt(1)
	v_mul_f32_e32 v27, v27, v249
	v_fmac_f32_e32 v27, v26, v248
	v_fmac_f32_e32 v27, v24, v250
	v_fmac_f32_e32 v27, v25, v251
	v_add_f32_e32 v23, v23, v27
	s_waitcnt lgkmcnt(0)
	v_mul_f32_e32 v15, v15, v253
	v_fmac_f32_e32 v15, v14, v252
	v_fmac_f32_e32 v15, v12, v254
	v_fmac_f32_e32 v15, v13, v255
	v_add_f32_e32 v12, v23, v15
	v_min_f32_e32 v13, 0, v12
	v_mul_f32_e64 v12, |v12|, s35
	v_exp_f32_e32 v12, v12
	v_mov_b32_e32 v24, 0
	v_add_f32_e32 v12, 1.0, v12
	v_cmp_gt_f32_e32 vcc, s21, v12
	s_nop 1
	v_cndmask_b32_e64 v14, 0, 32, vcc
	v_ldexp_f32 v12, v12, v14
	v_log_f32_e32 v12, v12
	s_nop 0
	v_mul_f32_e32 v14, 0x3f317217, v12
	v_fma_f32 v14, v12, s33, -v14
	v_fmac_f32_e32 v14, 0x3377d1cf, v12
	v_fmac_f32_e32 v14, 0x3f317217, v12
	v_cmp_lt_f32_e64 s[0:1], |v12|, s63
	s_nop 1
	v_cndmask_b32_e64 v12, v12, v14, s[0:1]
	v_cndmask_b32_e32 v14, 0, v215, vcc
	v_sub_f32_e32 v12, v12, v14
	v_sub_f32_e32 v12, v13, v12
	v_fmamk_f32 v23, v12, 0x3d800000, v63
	ds_write_b32 v42, v23 offset:32768
	s_waitcnt lgkmcnt(0)
	s_barrier
	ds_read2st64_b32 v[14:15], v45 offset0:128 offset1:130
	ds_read2st64_b32 v[12:13], v45 offset0:132 offset1:134
	s_waitcnt lgkmcnt(1)
	v_add_f32_e32 v15, v14, v15
	s_waitcnt lgkmcnt(0)
	v_add_f32_e32 v12, v15, v12
	s_and_saveexec_b64 s[0:1], s[40:41]
	s_cbranch_execz .LBB0_273
	v_cmp_lt_i32_e32 vcc, 1, v43
	s_mov_b64 s[6:7], 0
	s_and_saveexec_b64 s[8:9], vcc
	s_xor_b64 s[8:9], exec, s[8:9]
	s_cbranch_execz .LBB0_275
	v_cmp_eq_u32_e32 vcc, 2, v43
	s_mov_b64 s[6:7], -1
	s_and_saveexec_b64 s[10:11], vcc
	s_xor_b64 s[6:7], exec, -1
	s_or_b64 exec, exec, s[10:11]
	s_and_b64 s[6:7], s[6:7], exec
	v_readlane_b32 s84, v239, 39
	s_mov_b32 s85, 0xf800000
	s_andn2_saveexec_b64 s[8:9], s[8:9]
	s_cbranch_execnz .LBB0_276

.LBB0_366:
	s_or_b64 exec, exec, s[0:1]
	v_readlane_b32 s0, v239, 30
	s_waitcnt lgkmcnt(0)
	s_barrier
	v_mov_b32_e32 v1, s0
	ds_read_b32 v1, v1
	s_movk_i32 s0, 0x98f
	s_waitcnt lgkmcnt(0)
	v_cmp_lt_i32_e64 s[0:1], s0, v1
	v_readfirstlane_b32 s80, v1
	s_and_b64 vcc, exec, s[0:1]
	s_cbranch_vccnz .LBB0_361
	v_writelane_b32 v236, s0, 41
	s_cmpk_gt_i32 s80, 0x7f
	s_nop 0
	v_writelane_b32 v236, s1, 42
	s_mov_b64 s[0:1], -1
	s_cbranch_scc0 .LBB0_464
	s_cmpk_gt_u32 s80, 0x8f
	s_cbranch_scc0 .LBB0_450
	s_cmpk_gt_u32 s80, 0x18f
	s_cbranch_scc0 .LBB0_405
	s_cmpk_gt_u32 s80, 0x58f
	s_cbranch_scc0 .LBB0_402
	s_mov_b64 s[8:9], -1
	s_cmpk_gt_u32 s80, 0x78f
	s_cbranch_scc0 .LBB0_391
	v_mov_b32_e32 v4, v0
	s_movk_i32 s0, 0x100
	s_nop 0
	v_cmp_gt_i32_e32 vcc, s0, v4
	s_xor_b64 s[0:1], s[94:95], -1
	v_readfirstlane_b32 s10, v4
	s_and_b64 s[4:5], s[0:1], vcc
	s_and_saveexec_b64 s[0:1], s[4:5]
	s_cbranch_execz .LBB0_374
	v_ashrrev_i32_e32 v5, 31, v4
	v_readlane_b32 s4, v236, 27
	v_lshlrev_b64 v[10:11], 4, v[4:5]
	v_readlane_b32 s5, v236, 28
	v_lshl_add_u32 v1, v4, 4, 0
	s_nop 0
	v_lshl_add_u64 v[6:7], s[4:5], 0, v[10:11]
	global_load_dwordx4 v[6:9], v[6:7], off
	v_readlane_b32 s4, v236, 29
	v_readlane_b32 s5, v236, 30
	s_nop 1
	v_lshl_add_u64 v[240:241], s[4:5], 0, v[10:11]
	global_load_dwordx4 v[240:243], v[240:241], off
	v_readlane_b32 s4, v236, 31
	v_readlane_b32 s5, v236, 32
	s_nop 1
	v_lshl_add_u64 v[244:245], s[4:5], 0, v[10:11]
	global_load_dwordx4 v[244:247], v[244:245], off
	s_waitcnt vmcnt(2)
	ds_write_b128 v1, v[6:9]
	s_waitcnt vmcnt(1)
	ds_write_b128 v1, v[240:243] offset:4096
	s_waitcnt vmcnt(0)
	ds_write_b128 v1, v[244:247] offset:8192

.LBB0_408:
	s_lshl_b32 s0, s7, 5
	v_add_lshl_u32 v2, v101, s0, 9
	v_lshl_add_u64 v[12:13], v[2:3], 2, v[48:49]
	global_load_dwordx4 v[4:7], v[12:13], off offset:80
	global_load_dwordx4 v[8:11], v[12:13], off offset:64
	global_load_dwordx4 v[240:243], v[12:13], off offset:144
	global_load_dwordx4 v[244:247], v[12:13], off offset:128
	global_load_dwordx4 v[248:251], v[12:13], off offset:208
	global_load_dwordx4 v[252:255], v[12:13], off offset:192
	global_load_dwordx4 v[14:17], v[12:13], off offset:272
	global_load_dwordx4 v[36:39], v[12:13], off offset:256
	s_ashr_i32 s1, s0, 31
	v_lshl_add_u64 v[50:51], s[0:1], 2, v[46:47]
	s_mov_b32 s8, 0
	s_mov_b64 s[0:1], -1
	s_waitcnt vmcnt(7)
	v_cvt_pk_bf16_f32 v22, v4, v5
	v_cvt_pk_bf16_f32 v23, v6, v7
	s_waitcnt vmcnt(6)
	v_cvt_pk_bf16_f32 v20, v8, v9
	v_cvt_pk_bf16_f32 v21, v10, v11
	s_waitcnt vmcnt(5)
	v_cvt_pk_bf16_f32 v26, v240, v241
	v_cvt_pk_bf16_f32 v27, v242, v243
	s_waitcnt vmcnt(4)
	v_cvt_pk_bf16_f32 v24, v244, v245
	v_cvt_pk_bf16_f32 v25, v246, v247
	s_waitcnt vmcnt(3)
	v_cvt_pk_bf16_f32 v30, v248, v249
	v_cvt_pk_bf16_f32 v31, v250, v251
	s_waitcnt vmcnt(2)
	v_cvt_pk_bf16_f32 v28, v252, v253
	v_cvt_pk_bf16_f32 v29, v254, v255
	s_waitcnt vmcnt(1)
	v_cvt_pk_bf16_f32 v34, v14, v15
	v_cvt_pk_bf16_f32 v35, v16, v17
	s_waitcnt vmcnt(0)
	v_cvt_pk_bf16_f32 v32, v36, v37
	v_cvt_pk_bf16_f32 v33, v38, v39
